# removed 6 compiler-inserted vmcnt(0) flushes at GEMM K-loop preheaders (counted waits in loop suffice)
# speedup vs baseline: 1.0053x; 1.0053x over previous
;     ...
;         const char* nA = has_next ? ((GATHER ? gatherBase : nxt.A) + PG8_KOFS(nxt)) : cA; const char* nB = has_next ? (nxt.B + PG8_KOFS(nxt)) : cB;
;         for (int t = 0; t < nt; t += 2) {
;             const bool last = (t == nt - 2);
;             const char* a1 = cA + (size_t)(t + 1) * kstep;
;             const char* a2 = last ? nA : cA + (size_t)(t + 2) * kstep; const char* b2 = last ? nB : cB + (size_t)(t + 2) * kstep;
;             const char* a3 = a2 + kstep; const char* b3 = b2 + kstep;
;     ...
; #pragma unroll
;         for (int a = 0; a < 2; ++a)
; #pragma unroll
;             for (int b = 0; b < 2; ++b)
; #pragma unroll
;                 for (int m = 0; m < 4; ++m)
; #pragma unroll
;                     for (int n = 0; n < 2; ++n) acc[a][b][m][n] = (f32x4){0.f, 0.f, 0.f, 0.f};
;         cur = nxt; cA = nA; cB = nB; ++ui; nt = PG8_NT(cur);
.LBB0_543:
	s_and_b32 s21, s20, 3
	s_cmp_eq_u32 s21, 2
	s_cselect_b32 s26, 0x800, 0
	s_add_u32 s48, s36, s26
	s_addc_u32 s49, s37, 0
	s_and_b64 s[24:25], s[86:87], exec
	s_cselect_b32 s24, s49, s77
	s_cselect_b32 s25, s48, s76
	s_add_u32 s50, s38, s26
	s_addc_u32 s51, s39, 0
	s_and_b64 s[26:27], s[86:87], exec
	s_cselect_b32 s26, s51, s81
	s_cselect_b32 s27, s50, s80
	s_add_i32 s28, s22, -2
	s_add_u32 s76, s76, 0x80080
	s_addc_u32 s77, s77, 0
	s_add_u32 s29, s80, 0x100
	v_mov_b32_e32 v114, 0
	s_mov_b32 s31, 0
	s_addc_u32 s30, s81, 0
	v_mov_b32_e32 v115, v114
	v_mov_b32_e32 v116, v114
	v_mov_b32_e32 v117, v114
	v_mov_b32_e32 v118, v114
	v_mov_b32_e32 v119, v114
	v_mov_b32_e32 v120, v114
	v_mov_b32_e32 v121, v114
	v_mov_b32_e32 v98, v114
	v_mov_b32_e32 v99, v114
	v_mov_b32_e32 v100, v114
	v_mov_b32_e32 v101, v114
	v_mov_b32_e32 v102, v114
	v_mov_b32_e32 v103, v114
	v_mov_b32_e32 v104, v114
	v_mov_b32_e32 v105, v114
	v_mov_b32_e32 v82, v114
	v_mov_b32_e32 v83, v114
	v_mov_b32_e32 v84, v114
	v_mov_b32_e32 v85, v114
	v_mov_b32_e32 v86, v114
	v_mov_b32_e32 v87, v114
	v_mov_b32_e32 v88, v114
	v_mov_b32_e32 v89, v114
	v_mov_b32_e32 v66, v114
	v_mov_b32_e32 v67, v114
	v_mov_b32_e32 v68, v114
	v_mov_b32_e32 v69, v114
	v_mov_b32_e32 v70, v114
	v_mov_b32_e32 v71, v114
	v_mov_b32_e32 v72, v114
	v_mov_b32_e32 v73, v114
	v_mov_b32_e32 v122, v114
	v_mov_b32_e32 v123, v114
	v_mov_b32_e32 v124, v114
	v_mov_b32_e32 v125, v114
	v_mov_b32_e32 v126, v114
	v_mov_b32_e32 v127, v114
	v_mov_b32_e32 v128, v114
	v_mov_b32_e32 v129, v114
	v_mov_b32_e32 v106, v114
	v_mov_b32_e32 v107, v114
	v_mov_b32_e32 v108, v114
	v_mov_b32_e32 v109, v114
	v_mov_b32_e32 v110, v114
	v_mov_b32_e32 v111, v114
	v_mov_b32_e32 v112, v114
	v_mov_b32_e32 v113, v114
	v_mov_b32_e32 v90, v114
	v_mov_b32_e32 v91, v114
	v_mov_b32_e32 v92, v114
	v_mov_b32_e32 v93, v114
	v_mov_b32_e32 v94, v114
	v_mov_b32_e32 v95, v114
	v_mov_b32_e32 v96, v114
	v_mov_b32_e32 v97, v114
	v_mov_b32_e32 v74, v114
	v_mov_b32_e32 v75, v114
	v_mov_b32_e32 v76, v114
	v_mov_b32_e32 v77, v114
	v_mov_b32_e32 v78, v114
	v_mov_b32_e32 v79, v114
	v_mov_b32_e32 v80, v114
	v_mov_b32_e32 v81, v114
	v_mov_b32_e32 v50, v114
	v_mov_b32_e32 v51, v114
	v_mov_b32_e32 v52, v114
	v_mov_b32_e32 v53, v114
	v_mov_b32_e32 v54, v114
	v_mov_b32_e32 v55, v114
	v_mov_b32_e32 v56, v114
	v_mov_b32_e32 v57, v114
	v_mov_b32_e32 v34, v114
	v_mov_b32_e32 v35, v114
	v_mov_b32_e32 v36, v114
	v_mov_b32_e32 v37, v114
	v_mov_b32_e32 v38, v114
	v_mov_b32_e32 v39, v114
	v_mov_b32_e32 v40, v114
	v_mov_b32_e32 v41, v114
	v_mov_b32_e32 v18, v114
	v_mov_b32_e32 v19, v114
	v_mov_b32_e32 v20, v114
	v_mov_b32_e32 v21, v114
	v_mov_b32_e32 v22, v114
	v_mov_b32_e32 v23, v114
	v_mov_b32_e32 v24, v114
	v_mov_b32_e32 v25, v114
	v_mov_b32_e32 v2, v114
	v_mov_b32_e32 v3, v114
	v_mov_b32_e32 v4, v114
	v_mov_b32_e32 v5, v114
	v_mov_b32_e32 v6, v114
	v_mov_b32_e32 v7, v114
	v_mov_b32_e32 v8, v114
	v_mov_b32_e32 v9, v114
	v_mov_b32_e32 v58, v114
	v_mov_b32_e32 v59, v114
	v_mov_b32_e32 v60, v114
	v_mov_b32_e32 v61, v114
	v_mov_b32_e32 v62, v114
	v_mov_b32_e32 v63, v114
	v_mov_b32_e32 v64, v114
	v_mov_b32_e32 v65, v114
	v_mov_b32_e32 v42, v114
	v_mov_b32_e32 v43, v114
	v_mov_b32_e32 v44, v114
	v_mov_b32_e32 v45, v114
	v_mov_b32_e32 v46, v114
	v_mov_b32_e32 v47, v114
	v_mov_b32_e32 v48, v114
	v_mov_b32_e32 v49, v114
	v_mov_b32_e32 v26, v114
	v_mov_b32_e32 v27, v114
	v_mov_b32_e32 v28, v114
	v_mov_b32_e32 v29, v114
	v_mov_b32_e32 v30, v114
	v_mov_b32_e32 v31, v114
	v_mov_b32_e32 v32, v114
	v_mov_b32_e32 v33, v114
	v_mov_b32_e32 v10, v114
	v_mov_b32_e32 v11, v114
	v_mov_b32_e32 v12, v114
	v_mov_b32_e32 v13, v114
	v_mov_b32_e32 v14, v114
	v_mov_b32_e32 v15, v114
	v_mov_b32_e32 v16, v114
	v_mov_b32_e32 v17, v114

;     ...
; #pragma unroll
;         for (int a = 0; a < 2; ++a)
; #pragma unroll
;             for (int b = 0; b < 2; ++b)
; #pragma unroll
;                 for (int m = 0; m < 4; ++m)
; #pragma unroll
;                     for (int n = 0; n < 2; ++n) acc[a][b][m][n] = (f32x4){0.f, 0.f, 0.f, 0.f};
;         cur = nxt; cA = nA; cB = nB; ++ui; nt = PG8_NT(cur);
.LBB0_1084:
	s_add_u32 s48, s48, 0x80080
	s_addc_u32 s49, s49, 0
	s_add_u32 s13, s50, 0x100
	v_mov_b32_e32 v2, 0
	s_addc_u32 s14, s51, 0
	s_mov_b32 s15, -2
	v_mov_b32_e32 v3, v2
	v_mov_b32_e32 v4, v2
	v_mov_b32_e32 v5, v2
	v_mov_b32_e32 v6, v2
	v_mov_b32_e32 v7, v2
	v_mov_b32_e32 v8, v2
	v_mov_b32_e32 v9, v2
	v_mov_b32_e32 v18, v2
	v_mov_b32_e32 v19, v2
	v_mov_b32_e32 v20, v2
	v_mov_b32_e32 v21, v2
	v_mov_b32_e32 v22, v2
	v_mov_b32_e32 v23, v2
	v_mov_b32_e32 v24, v2
	v_mov_b32_e32 v25, v2
	v_mov_b32_e32 v34, v2
	v_mov_b32_e32 v35, v2
	v_mov_b32_e32 v36, v2
	v_mov_b32_e32 v37, v2
	v_mov_b32_e32 v38, v2
	v_mov_b32_e32 v39, v2
	v_mov_b32_e32 v40, v2
	v_mov_b32_e32 v41, v2
	v_mov_b32_e32 v50, v2
	v_mov_b32_e32 v51, v2
	v_mov_b32_e32 v52, v2
	v_mov_b32_e32 v53, v2
	v_mov_b32_e32 v54, v2
	v_mov_b32_e32 v55, v2
	v_mov_b32_e32 v56, v2
	v_mov_b32_e32 v57, v2
	v_mov_b32_e32 v10, v2
	v_mov_b32_e32 v11, v2
	v_mov_b32_e32 v12, v2
	v_mov_b32_e32 v13, v2
	v_mov_b32_e32 v14, v2
	v_mov_b32_e32 v15, v2
	v_mov_b32_e32 v16, v2
	v_mov_b32_e32 v17, v2
	v_mov_b32_e32 v26, v2
	v_mov_b32_e32 v27, v2
	v_mov_b32_e32 v28, v2
	v_mov_b32_e32 v29, v2
	v_mov_b32_e32 v30, v2
	v_mov_b32_e32 v31, v2
	v_mov_b32_e32 v32, v2
	v_mov_b32_e32 v33, v2
	v_mov_b32_e32 v42, v2
	v_mov_b32_e32 v43, v2
	v_mov_b32_e32 v44, v2
	v_mov_b32_e32 v45, v2
	v_mov_b32_e32 v46, v2
	v_mov_b32_e32 v47, v2
	v_mov_b32_e32 v48, v2
	v_mov_b32_e32 v49, v2
	v_mov_b32_e32 v58, v2
	v_mov_b32_e32 v59, v2
	v_mov_b32_e32 v60, v2
	v_mov_b32_e32 v61, v2
	v_mov_b32_e32 v62, v2
	v_mov_b32_e32 v63, v2
	v_mov_b32_e32 v64, v2
	v_mov_b32_e32 v65, v2
	v_mov_b32_e32 v66, v2
	v_mov_b32_e32 v67, v2
	v_mov_b32_e32 v68, v2
	v_mov_b32_e32 v69, v2
	v_mov_b32_e32 v70, v2
	v_mov_b32_e32 v71, v2
	v_mov_b32_e32 v72, v2
	v_mov_b32_e32 v73, v2
	v_mov_b32_e32 v82, v2
	v_mov_b32_e32 v83, v2
	v_mov_b32_e32 v84, v2
	v_mov_b32_e32 v85, v2
	v_mov_b32_e32 v86, v2
	v_mov_b32_e32 v87, v2
	v_mov_b32_e32 v88, v2
	v_mov_b32_e32 v89, v2
	v_mov_b32_e32 v98, v2
	v_mov_b32_e32 v99, v2
	v_mov_b32_e32 v100, v2
	v_mov_b32_e32 v101, v2
	v_mov_b32_e32 v102, v2
	v_mov_b32_e32 v103, v2
	v_mov_b32_e32 v104, v2
	v_mov_b32_e32 v105, v2
	v_mov_b32_e32 v114, v2
	v_mov_b32_e32 v115, v2
	v_mov_b32_e32 v116, v2
	v_mov_b32_e32 v117, v2
	v_mov_b32_e32 v118, v2
	v_mov_b32_e32 v119, v2
	v_mov_b32_e32 v120, v2
	v_mov_b32_e32 v121, v2
	v_mov_b32_e32 v74, v2
	v_mov_b32_e32 v75, v2
	v_mov_b32_e32 v76, v2
	v_mov_b32_e32 v77, v2
	v_mov_b32_e32 v78, v2
	v_mov_b32_e32 v79, v2
	v_mov_b32_e32 v80, v2
	v_mov_b32_e32 v81, v2
	v_mov_b32_e32 v90, v2
	v_mov_b32_e32 v91, v2
	v_mov_b32_e32 v92, v2
	v_mov_b32_e32 v93, v2
	v_mov_b32_e32 v94, v2
	v_mov_b32_e32 v95, v2
	v_mov_b32_e32 v96, v2
	v_mov_b32_e32 v97, v2
	v_mov_b32_e32 v106, v2
	v_mov_b32_e32 v107, v2
	v_mov_b32_e32 v108, v2
	v_mov_b32_e32 v109, v2
	v_mov_b32_e32 v110, v2
	v_mov_b32_e32 v111, v2
	v_mov_b32_e32 v112, v2
	v_mov_b32_e32 v113, v2
	v_mov_b32_e32 v122, v2
	v_mov_b32_e32 v123, v2
	v_mov_b32_e32 v124, v2
	v_mov_b32_e32 v125, v2
	v_mov_b32_e32 v126, v2
	v_mov_b32_e32 v127, v2
	v_mov_b32_e32 v128, v2
	v_mov_b32_e32 v129, v2

;     ...
; #pragma unroll
;         for (int a = 0; a < 2; ++a)
; #pragma unroll
;             for (int b = 0; b < 2; ++b)
; #pragma unroll
;                 for (int m = 0; m < 4; ++m)
; #pragma unroll
;                     for (int n = 0; n < 2; ++n) acc[a][b][m][n] = (f32x4){0.f, 0.f, 0.f, 0.f};
;         cur = nxt; cA = nA; cB = nB; ++ui; nt = PG8_NT(cur);
.LBB0_1116:
	s_add_u32 s48, s48, 0x80080
	s_addc_u32 s49, s49, 0
	s_add_u32 s13, s50, 0x100
	v_mov_b32_e32 v2, 0
	s_addc_u32 s14, s51, 0
	s_mov_b32 s15, -2
	v_mov_b32_e32 v3, v2
	v_mov_b32_e32 v4, v2
	v_mov_b32_e32 v5, v2
	v_mov_b32_e32 v6, v2
	v_mov_b32_e32 v7, v2
	v_mov_b32_e32 v8, v2
	v_mov_b32_e32 v9, v2
	v_mov_b32_e32 v14, v2
	v_mov_b32_e32 v15, v2
	v_mov_b32_e32 v16, v2
	v_mov_b32_e32 v17, v2
	v_mov_b32_e32 v22, v2
	v_mov_b32_e32 v23, v2
	v_mov_b32_e32 v24, v2
	v_mov_b32_e32 v25, v2
	v_mov_b32_e32 v34, v2
	v_mov_b32_e32 v35, v2
	v_mov_b32_e32 v36, v2
	v_mov_b32_e32 v37, v2
	v_mov_b32_e32 v38, v2
	v_mov_b32_e32 v39, v2
	v_mov_b32_e32 v40, v2
	v_mov_b32_e32 v41, v2
	v_mov_b32_e32 v46, v2
	v_mov_b32_e32 v47, v2
	v_mov_b32_e32 v48, v2
	v_mov_b32_e32 v49, v2
	v_mov_b32_e32 v54, v2
	v_mov_b32_e32 v55, v2
	v_mov_b32_e32 v56, v2
	v_mov_b32_e32 v57, v2
	v_mov_b32_e32 v10, v2
	v_mov_b32_e32 v11, v2
	v_mov_b32_e32 v12, v2
	v_mov_b32_e32 v13, v2
	v_mov_b32_e32 v18, v2
	v_mov_b32_e32 v19, v2
	v_mov_b32_e32 v20, v2
	v_mov_b32_e32 v21, v2
	v_mov_b32_e32 v26, v2
	v_mov_b32_e32 v27, v2
	v_mov_b32_e32 v28, v2
	v_mov_b32_e32 v29, v2
	v_mov_b32_e32 v30, v2
	v_mov_b32_e32 v31, v2
	v_mov_b32_e32 v32, v2
	v_mov_b32_e32 v33, v2
	v_mov_b32_e32 v42, v2
	v_mov_b32_e32 v43, v2
	v_mov_b32_e32 v44, v2
	v_mov_b32_e32 v45, v2
	v_mov_b32_e32 v50, v2
	v_mov_b32_e32 v51, v2
	v_mov_b32_e32 v52, v2
	v_mov_b32_e32 v53, v2
	v_mov_b32_e32 v58, v2
	v_mov_b32_e32 v59, v2
	v_mov_b32_e32 v60, v2
	v_mov_b32_e32 v61, v2
	v_mov_b32_e32 v62, v2
	v_mov_b32_e32 v63, v2
	v_mov_b32_e32 v64, v2
	v_mov_b32_e32 v65, v2
	v_mov_b32_e32 v66, v2
	v_mov_b32_e32 v67, v2
	v_mov_b32_e32 v68, v2
	v_mov_b32_e32 v69, v2
	v_mov_b32_e32 v70, v2
	v_mov_b32_e32 v71, v2
	v_mov_b32_e32 v72, v2
	v_mov_b32_e32 v73, v2
	v_mov_b32_e32 v78, v2
	v_mov_b32_e32 v79, v2
	v_mov_b32_e32 v80, v2
	v_mov_b32_e32 v81, v2
	v_mov_b32_e32 v86, v2
	v_mov_b32_e32 v87, v2
	v_mov_b32_e32 v88, v2
	v_mov_b32_e32 v89, v2
	v_mov_b32_e32 v98, v2
	v_mov_b32_e32 v99, v2
	v_mov_b32_e32 v100, v2
	v_mov_b32_e32 v101, v2
	v_mov_b32_e32 v102, v2
	v_mov_b32_e32 v103, v2
	v_mov_b32_e32 v104, v2
	v_mov_b32_e32 v105, v2
	v_mov_b32_e32 v110, v2
	v_mov_b32_e32 v111, v2
	v_mov_b32_e32 v112, v2
	v_mov_b32_e32 v113, v2
	v_mov_b32_e32 v118, v2
	v_mov_b32_e32 v119, v2
	v_mov_b32_e32 v120, v2
	v_mov_b32_e32 v121, v2
	v_mov_b32_e32 v74, v2
	v_mov_b32_e32 v75, v2
	v_mov_b32_e32 v76, v2
	v_mov_b32_e32 v77, v2
	v_mov_b32_e32 v82, v2
	v_mov_b32_e32 v83, v2
	v_mov_b32_e32 v84, v2
	v_mov_b32_e32 v85, v2
	v_mov_b32_e32 v90, v2
	v_mov_b32_e32 v91, v2
	v_mov_b32_e32 v92, v2
	v_mov_b32_e32 v93, v2
	v_mov_b32_e32 v94, v2
	v_mov_b32_e32 v95, v2
	v_mov_b32_e32 v96, v2
	v_mov_b32_e32 v97, v2
	v_mov_b32_e32 v106, v2
	v_mov_b32_e32 v107, v2
	v_mov_b32_e32 v108, v2
	v_mov_b32_e32 v109, v2
	v_mov_b32_e32 v114, v2
	v_mov_b32_e32 v115, v2
	v_mov_b32_e32 v116, v2
	v_mov_b32_e32 v117, v2
	v_mov_b32_e32 v122, v2
	v_mov_b32_e32 v123, v2
	v_mov_b32_e32 v124, v2
	v_mov_b32_e32 v125, v2
	v_mov_b32_e32 v126, v2
	v_mov_b32_e32 v127, v2
	v_mov_b32_e32 v128, v2
	v_mov_b32_e32 v129, v2

; #define SB() __builtin_amdgcn_sched_barrier(0)
; #define PG8_STAGE(bufoff, gbase, voff) do { _Pragma("unroll") for (int _i = 0; _i < 2; ++_i) \
;         __builtin_amdgcn_global_load_lds((const unsigned*)((const char*)(gbase) + (voff)[_i]), (LAS unsigned*)(lds + (bufoff) + ldsw + _i * 8192), 16, 0, 0); } while (0)
; #define PG8_WAIT_V(n) asm volatile("s_waitcnt vmcnt(" #n ")" ::: "memory")
; #define PG8_BAR __builtin_amdgcn_s_barrier()
;     ...
;     for (int i = 0; i < 2; ++i) { int R, C; stage_rc(tid * 16 + i * 8192, R, C); const int Rb = Epi::PERM ? ((R & ~31) + perm32(R & 31)) : R;
;         voffA[i] = (unsigned)R * lda + (unsigned)C * 2u; voffB[i] = (unsigned)Rb * ldb + (unsigned)C * 2u; RA[i] = R; CA2[i] = (unsigned)C * 2u; }
;     const size_t kstep = (size_t)(BK * 2);
;     const size_t hstepA = GATHER ? 0 : (size_t)HALF * lda, hstepB = (size_t)HALF * ldb;
;     const unsigned ldsw = (unsigned)wid * 1024u;
;     const int aoff = lds_byte(wr * 64 + fr, fq * 8), boff = lds_byte(wc * 32 + fr, fq * 8);
;     unsigned cg[2], ng[2];
;     ...
;     Unit cur, nxt; int ui = 0;
;     if (!S.next(0, cur)) return;
;     if constexpr (GATHER) {
;         { const unsigned t0 = (unsigned)S.rowtok(cur, RA[0]), t1 = (unsigned)S.rowtok(cur, RA[1]), t2 = (unsigned)S.rowtok(cur, HALF + RA[0]), t3 = (unsigned)S.rowtok(cur, HALF + RA[1]);
;           SB(); cg[0] = t0 | (t1 << 16); cg[1] = t2 | (t3 << 16); }
;     }
;     f32x4 acc[2][2][4][2];
; #pragma unroll
;     for (int a = 0; a < 2; ++a)
; #pragma unroll
;         for (int b = 0; b < 2; ++b)
; #pragma unroll
;             for (int m = 0; m < 4; ++m)
; #pragma unroll
;                 for (int n = 0; n < 2; ++n) acc[a][b][m][n] = (f32x4){0.f, 0.f, 0.f, 0.f};
;     bf16x8 At[4][2], B0[2][2], B1[2][2];
;     const char* cA = (GATHER ? gatherBase : cur.A) + PG8_KOFS(cur); const char* cB = cur.B + PG8_KOFS(cur); int nt = PG8_NT(cur);
;     PG8_STAGE(PG8_SB(0, 0), cB, voffB); PG8_STAGE(PG8_SB(0, 1), cB + hstepB, voffB); PG8_STAGE_A(PG8_SA(0, 0), 0, cA, false); PG8_STAGE_A(PG8_SA(0, 1), 1, cA, false);
;     if (wr == 1) PG8_BAR;
;     PG8_WAIT_V(2); PG8_BAR;
;     PG8_STAGE(PG8_SB(1, 0), cB + kstep, voffB); PG8_STAGE_A(PG8_SA(1, 0), 0, cA + kstep, false); PG8_STAGE(PG8_SB(1, 1), cB + hstepB + kstep, voffB);
;     PG8_WAIT_V(6); PG8_BAR;
.LBB0_1191:
	s_add_u32 s14, s14, 0x2de81000
	s_addc_u32 s15, s15, 0
	s_lshl_b64 s[4:5], s[4:5], 9
	s_add_u32 s16, s14, s36
	s_addc_u32 s17, s15, s37
	s_add_u32 s40, s16, s4
	s_addc_u32 s41, s17, s5
	v_lshl_add_u64 v[2:3], v[2:3], 0, s[92:93]
	s_add_i32 m0, s10, 0x18000
	s_waitcnt vmcnt(2)
	s_barrier
	global_load_lds_dwordx4 v[2:3], off
	v_lshl_add_u64 v[2:3], v[4:5], 0, s[92:93]
	s_add_i32 m0, s10, 0x1a000
	s_add_i32 s16, s10, 0x8000
	s_add_i32 s17, s10, 0xa000
	global_load_lds_dwordx4 v[2:3], off
	v_lshl_add_u64 v[2:3], v[6:7], 0, s[92:93]
	s_mov_b32 m0, s16
	s_add_u32 s4, s46, 0x80080
	global_load_lds_dwordx4 v[2:3], off
	v_lshl_add_u64 v[2:3], v[8:9], 0, s[92:93]
	s_mov_b32 m0, s17
	s_addc_u32 s5, s47, 0
	global_load_lds_dwordx4 v[2:3], off
	v_lshl_add_u64 v[2:3], s[4:5], 0, v[0:1]
	s_add_i32 m0, s10, 0x1c000
	v_and_b32_e32 v146, 15, v10
	global_load_lds_dwordx4 v[2:3], off
	v_lshl_add_u64 v[2:3], s[4:5], 0, v[134:135]
	s_add_i32 m0, s10, 0x1e000
	v_and_b32_e32 v5, 48, v10
	global_load_lds_dwordx4 v[2:3], off
	v_or_b32_e32 v2, s33, v146
	v_ashrrev_i32_e32 v3, 1, v10
	v_lshlrev_b32_e32 v4, 6, v2
	s_movk_i32 s4, 0x3c0
	v_and_b32_e32 v136, -8, v3
	v_ashrrev_i32_e32 v3, 6, v10
	v_and_or_b32 v4, v4, s4, v5
	v_readlane_b32 s4, v252, 10
	v_lshlrev_b32_e32 v2, 2, v2
	v_and_b32_e32 v2, 32, v2
	v_lshl_add_u32 v6, v3, 10, s4
	v_bitop3_b32 v2, v4, v6, v2 bitop3:0xde
	v_lshl_or_b32 v4, v146, 6, v5
	v_readlane_b32 s4, v252, 11
	v_lshlrev_b32_e32 v5, 2, v10
	v_and_b32_e32 v5, 32, v5
	v_add_lshl_u32 v3, v3, s4, 10
	v_bitop3_b32 v147, v4, v3, v5 bitop3:0xde
	v_lshlrev_b32_e32 v3, 15, v11
	v_and_b32_e32 v3, 0xffff0000, v3
	v_lshl_add_u32 v3, v12, 12, v3
	v_and_b32_e32 v4, 1, v11
	v_lshl_or_b32 v3, v4, 6, v3
	v_lshl_add_u32 v138, v13, 1, v3
	v_lshlrev_b32_e32 v3, 15, v14
	v_and_b32_e32 v3, 0xffff0000, v3
	s_waitcnt vmcnt(6)
	v_lshl_add_u32 v3, v15, 12, v3
	v_and_b32_e32 v4, 1, v14
	v_lshl_or_b32 v3, v4, 6, v3
	v_ashrrev_i32_e32 v137, 31, v136
	v_mov_b32_e32 v139, v1
	v_lshl_add_u32 v140, v16, 1, v3
	v_mov_b32_e32 v141, v1
	s_mov_b32 s20, 0
	v_add_u32_e32 v148, 0, v2
	s_barrier
	s_branch .LBB0_1194

;     ...
; #pragma unroll
;         for (int a = 0; a < 2; ++a)
; #pragma unroll
;             for (int b = 0; b < 2; ++b)
; #pragma unroll
;                 for (int m = 0; m < 4; ++m)
; #pragma unroll
;                     for (int n = 0; n < 2; ++n) acc[a][b][m][n] = (f32x4){0.f, 0.f, 0.f, 0.f};
;         cur = nxt; cA = nA; cB = nB; ++ui; nt = PG8_NT(cur);
.LBB0_1391:
	s_add_u32 s48, s48, 0x40080
	s_addc_u32 s49, s49, 0
	s_add_u32 s17, s50, 0x100
	v_mov_b32_e32 v2, 0
	s_addc_u32 s18, s51, 0
	s_mov_b32 s19, -2
	v_mov_b32_e32 v3, v2
	v_mov_b32_e32 v4, v2
	v_mov_b32_e32 v5, v2
	v_mov_b32_e32 v6, v2
	v_mov_b32_e32 v7, v2
	v_mov_b32_e32 v8, v2
	v_mov_b32_e32 v9, v2
	v_mov_b32_e32 v18, v2
	v_mov_b32_e32 v19, v2
	v_mov_b32_e32 v20, v2
	v_mov_b32_e32 v21, v2
	v_mov_b32_e32 v22, v2
	v_mov_b32_e32 v23, v2
	v_mov_b32_e32 v24, v2
	v_mov_b32_e32 v25, v2
	v_mov_b32_e32 v34, v2
	v_mov_b32_e32 v35, v2
	v_mov_b32_e32 v36, v2
	v_mov_b32_e32 v37, v2
	v_mov_b32_e32 v38, v2
	v_mov_b32_e32 v39, v2
	v_mov_b32_e32 v40, v2
	v_mov_b32_e32 v41, v2
	v_mov_b32_e32 v50, v2
	v_mov_b32_e32 v51, v2
	v_mov_b32_e32 v52, v2
	v_mov_b32_e32 v53, v2
	v_mov_b32_e32 v54, v2
	v_mov_b32_e32 v55, v2
	v_mov_b32_e32 v56, v2
	v_mov_b32_e32 v57, v2
	v_mov_b32_e32 v10, v2
	v_mov_b32_e32 v11, v2
	v_mov_b32_e32 v12, v2
	v_mov_b32_e32 v13, v2
	v_mov_b32_e32 v14, v2
	v_mov_b32_e32 v15, v2
	v_mov_b32_e32 v16, v2
	v_mov_b32_e32 v17, v2
	v_mov_b32_e32 v26, v2
	v_mov_b32_e32 v27, v2
	v_mov_b32_e32 v28, v2
	v_mov_b32_e32 v29, v2
	v_mov_b32_e32 v30, v2
	v_mov_b32_e32 v31, v2
	v_mov_b32_e32 v32, v2
	v_mov_b32_e32 v33, v2
	v_mov_b32_e32 v42, v2
	v_mov_b32_e32 v43, v2
	v_mov_b32_e32 v44, v2
	v_mov_b32_e32 v45, v2
	v_mov_b32_e32 v46, v2
	v_mov_b32_e32 v47, v2
	v_mov_b32_e32 v48, v2
	v_mov_b32_e32 v49, v2
	v_mov_b32_e32 v58, v2
	v_mov_b32_e32 v59, v2
	v_mov_b32_e32 v60, v2
	v_mov_b32_e32 v61, v2
	v_mov_b32_e32 v62, v2
	v_mov_b32_e32 v63, v2
	v_mov_b32_e32 v64, v2
	v_mov_b32_e32 v65, v2
	v_mov_b32_e32 v66, v2
	v_mov_b32_e32 v67, v2
	v_mov_b32_e32 v68, v2
	v_mov_b32_e32 v69, v2
	v_mov_b32_e32 v70, v2
	v_mov_b32_e32 v71, v2
	v_mov_b32_e32 v72, v2
	v_mov_b32_e32 v73, v2
	v_mov_b32_e32 v82, v2
	v_mov_b32_e32 v83, v2
	v_mov_b32_e32 v84, v2
	v_mov_b32_e32 v85, v2
	v_mov_b32_e32 v86, v2
	v_mov_b32_e32 v87, v2
	v_mov_b32_e32 v88, v2
	v_mov_b32_e32 v89, v2
	v_mov_b32_e32 v98, v2
	v_mov_b32_e32 v99, v2
	v_mov_b32_e32 v100, v2
	v_mov_b32_e32 v101, v2
	v_mov_b32_e32 v102, v2
	v_mov_b32_e32 v103, v2
	v_mov_b32_e32 v104, v2
	v_mov_b32_e32 v105, v2
	v_mov_b32_e32 v114, v2
	v_mov_b32_e32 v115, v2
	v_mov_b32_e32 v116, v2
	v_mov_b32_e32 v117, v2
	v_mov_b32_e32 v118, v2
	v_mov_b32_e32 v119, v2
	v_mov_b32_e32 v120, v2
	v_mov_b32_e32 v121, v2
	v_mov_b32_e32 v74, v2
	v_mov_b32_e32 v75, v2
	v_mov_b32_e32 v76, v2
	v_mov_b32_e32 v77, v2
	v_mov_b32_e32 v78, v2
	v_mov_b32_e32 v79, v2
	v_mov_b32_e32 v80, v2
	v_mov_b32_e32 v81, v2
	v_mov_b32_e32 v90, v2
	v_mov_b32_e32 v91, v2
	v_mov_b32_e32 v92, v2
	v_mov_b32_e32 v93, v2
	v_mov_b32_e32 v94, v2
	v_mov_b32_e32 v95, v2
	v_mov_b32_e32 v96, v2
	v_mov_b32_e32 v97, v2
	v_mov_b32_e32 v106, v2
	v_mov_b32_e32 v107, v2
	v_mov_b32_e32 v108, v2
	v_mov_b32_e32 v109, v2
	v_mov_b32_e32 v110, v2
	v_mov_b32_e32 v111, v2
	v_mov_b32_e32 v112, v2
	v_mov_b32_e32 v113, v2
	v_mov_b32_e32 v122, v2
	v_mov_b32_e32 v123, v2
	v_mov_b32_e32 v124, v2
	v_mov_b32_e32 v125, v2
	v_mov_b32_e32 v126, v2
	v_mov_b32_e32 v127, v2
	v_mov_b32_e32 v128, v2
	v_mov_b32_e32 v129, v2

; #define PG8_STAGE(bufoff, gbase, voff) do { _Pragma("unroll") for (int _i = 0; _i < 2; ++_i) \
;         __builtin_amdgcn_global_load_lds((const unsigned*)((const char*)(gbase) + (voff)[_i]), (LAS unsigned*)(lds + (bufoff) + ldsw + _i * 8192), 16, 0, 0); } while (0)
; #define PG8_STAGE_A(bufoff, h, kp, nx) do { if constexpr (GATHER) { const unsigned _p = (nx) ? ng[h] : cg[h]; unsigned _v[2]; _v[0] = (_p & 0xffffu) * lda + CA2[0]; _v[1] = (_p >> 16) * lda + CA2[1]; PG8_STAGE(bufoff, kp, _v); } \
;         else { PG8_STAGE(bufoff, (kp) + (h) * hstepA, voffA); } } while (0)
; #define PG8_WAIT_V(n) asm volatile("s_waitcnt vmcnt(" #n ")" ::: "memory")
; #define PG8_BAR __builtin_amdgcn_s_barrier()
; __device__ __forceinline__ int xcd_remap(int L, int nwg) { const int q = nwg / 8, r = nwg % 8, xcd = L % 8, off = L / 8; return (xcd < r ? xcd * (q + 1) : r * (q + 1) + (xcd - r) * q) + off; }
;     ...
;     PG8_STAGE(PG8_SB(0, 0), cB, voffB); PG8_STAGE(PG8_SB(0, 1), cB + hstepB, voffB); PG8_STAGE_A(PG8_SA(0, 0), 0, cA, false); PG8_STAGE_A(PG8_SA(0, 1), 1, cA, false);
;     if (wr == 1) PG8_BAR;
;     PG8_WAIT_V(2); PG8_BAR;
;     PG8_STAGE(PG8_SB(1, 0), cB + kstep, voffB); PG8_STAGE_A(PG8_SA(1, 0), 0, cA + kstep, false); PG8_STAGE(PG8_SB(1, 1), cB + hstepB + kstep, voffB);
;     PG8_WAIT_V(6); PG8_BAR;
;     __device__ __forceinline__ bool next(int i, pg8::Unit& u) const {
;     ...
;         const int w = xcd_remap(L, nu), g = t0 + (w >> 3), ct = w & 7; int am = 3;
;         const int e = __builtin_amdgcn_readfirstlane((int)M[MT_TE + g]); const int rt = __builtin_amdgcn_readfirstlane((int)M[MT_TR + g]);
;         if ((int)M[MT_CNT + e] - rt * 256 <= 128) am &= 1;
;         u.amask = am;
;         u.A = H + (size_t)g * 256 * FH * 2; u.B = W2 + ((size_t)e * D + 256 * ct) * FH * 2; u.C = Y + ((size_t)g * 256 * D + 256 * ct) * 2; u.ldc = D; u.row0 = g * 256; u.e0 = e; u.e1 = 0; return true;
.LBB0_1620:
	s_add_u32 s23, s44, 0x225c1000
	s_addc_u32 s24, s45, 0
	s_lshl_b32 s26, s26, 8
	s_sub_i32 s26, s27, s26
	s_cmpk_lt_i32 s26, 0x81
	s_cselect_b32 s52, 1, 3
	s_lshl_b64 s[4:5], s[4:5], 20
	s_lshl_b32 s26, s28, 1
	s_add_u32 s4, s23, s4
	s_addc_u32 s5, s24, s5
	s_add_u32 s44, s4, s26
	s_addc_u32 s45, s5, 0
	s_add_i32 s26, s15, 0x18000
	v_lshl_add_u64 v[2:3], v[2:3], 0, s[92:93]
	s_mov_b32 m0, s26
	s_add_i32 s27, s15, 0x1a000
	s_sub_i32 s25, s68, s25
	s_waitcnt vmcnt(2)
	s_barrier
	global_load_lds_dwordx4 v[2:3], off
	v_lshl_add_u64 v[2:3], v[4:5], 0, s[92:93]
	s_mov_b32 m0, s27
	s_add_i32 s28, s15, 0x8000
	s_add_i32 s29, s15, 0xa000
	global_load_lds_dwordx4 v[2:3], off
	v_lshl_add_u64 v[2:3], v[6:7], 0, s[92:93]
	s_mov_b32 m0, s28
	s_add_u32 s4, s58, 0x20080
	global_load_lds_dwordx4 v[2:3], off
	v_lshl_add_u64 v[2:3], v[8:9], 0, s[92:93]
	s_mov_b32 m0, s29
	s_addc_u32 s5, s59, 0
	s_add_i32 s30, s15, 0x1c000
	global_load_lds_dwordx4 v[2:3], off
	v_lshl_add_u64 v[2:3], s[4:5], 0, v[200:201]
	s_mov_b32 m0, s30
	s_add_i32 s31, s15, 0x1e000
	global_load_lds_dwordx4 v[2:3], off
	v_lshl_add_u64 v[2:3], s[4:5], 0, v[196:197]
	s_mov_b32 m0, s31
	v_and_b32_e32 v223, 15, v0
	global_load_lds_dwordx4 v[2:3], off
	v_or_b32_e32 v2, s33, v223
	v_ashrrev_i32_e32 v3, 1, v0
	v_lshlrev_b32_e32 v4, 6, v2
	v_and_b32_e32 v5, 48, v0
	s_movk_i32 s4, 0x3c0
	v_and_b32_e32 v204, -8, v3
	v_ashrrev_i32_e32 v3, 6, v0
	v_and_or_b32 v4, v4, s4, v5
	v_readlane_b32 s4, v252, 10
	v_lshlrev_b32_e32 v2, 2, v2
	v_and_b32_e32 v2, 32, v2
	v_lshl_add_u32 v6, v3, 10, s4
	v_readlane_b32 s4, v252, 11
	v_lshlrev_b32_e32 v0, 2, v0
	v_bitop3_b32 v2, v4, v6, v2 bitop3:0xde
	v_lshl_or_b32 v4, v223, 6, v5
	v_add_lshl_u32 v3, v3, s4, 10
	v_and_b32_e32 v0, 32, v0
	v_bitop3_b32 v0, v4, v3, v0 bitop3:0xde
	v_lshlrev_b32_e32 v3, 13, v13
	v_and_b32_e32 v3, 0xffffc000, v3
	v_lshl_add_u32 v3, v14, 10, v3
	v_and_b32_e32 v4, 1, v13
	v_lshl_or_b32 v3, v4, 6, v3
	v_lshl_add_u32 v206, v15, 1, v3
	v_lshlrev_b32_e32 v3, 13, v10
	v_and_b32_e32 v3, 0xffffc000, v3
	s_waitcnt vmcnt(6)
	v_lshl_add_u32 v3, v11, 10, v3
	v_and_b32_e32 v4, 1, v10
	v_lshl_or_b32 v3, v4, 6, v3
	v_ashrrev_i32_e32 v205, 31, v204
	v_mov_b32_e32 v207, v1
	v_lshl_add_u32 v208, v12, 1, v3
	v_mov_b32_e32 v209, v1
	s_mov_b32 s34, 0
	v_add_u32_e32 v224, 0, v0
	v_add_u32_e32 v225, 0, v2
	s_barrier
	s_branch .LBB0_1622
